# K2: kp VALU chain moved into the MFMA shadow (MFMA/VALU interleave)
# baseline (speedup 1.0000x reference)
_Z9k2_layer1PKfS0_S0_PfS1_S1_:
	s_load_dwordx8 s[4:11], s[0:1], 0x0
	s_load_dwordx4 s[12:15], s[0:1], 0x20
	s_lshr_b32 s16, s2, 5
	s_and_b32 s17, s2, 31
	s_lshl_b32 s17, s17, 4
	s_movk_i32 s18, 0x500
	v_and_b32_e32 v1, 15, v0
	v_lshrrev_b32_e32 v2, 4, v0
	v_lshl_add_u32 v3, s16, 4, v2
	v_add_u32_e32 v4, s17, v1
	v_lshlrev_b32_e32 v4, 2, v4
	v_lshl_add_u32 v5, v3, 11, v4
	v_add_u32_e32 v6, 0x40000, v5
	v_lshl_add_u32 v7, v3, 14, v4
	v_add_u32_e32 v7, 0x80000, v7
	v_add_u32_e32 v8, 0x1000, v7
	v_add_u32_e32 v9, 0x2000, v7
	v_add_u32_e32 v10, 0x3000, v7
	v_and_b32_e32 v11, 7, v1
	v_lshl_add_u32 v11, v3, 3, v11
	v_lshlrev_b32_e32 v11, 2, v11
	v_and_b32_e32 v12, 8, v1
	v_lshl_add_u32 v11, v12, 9, v11
	v_add_u32_e32 v11, 0x280000, v11
	v_lshrrev_b32_e32 v13, 6, v0
	v_bfe_u32 v14, v0, 4, 2
	v_lshl_add_u32 v15, v13, 4, v1
	v_mul_u32_u24_e32 v16, 20, v15
	v_mad_u32_u24 v16, v14, s18, v16
	v_add_u32_e32 v17, 0x1400, v16
	v_add_u32_e32 v18, 0x2800, v16
	v_add_u32_e32 v19, 0x3c00, v16
	v_lshlrev_b32_e32 v20, 2, v15
	s_lshl_b32 s19, s2, 4
	v_add_u32_e32 v59, s19, v1
	v_lshlrev_b32_e32 v59, 6, v59
	v_lshl_add_u32 v59, v13, 4, v59
	v_lshl_add_u32 v59, v14, 2, v59
	v_lshlrev_b32_e32 v59, 2, v59
	v_and_b32_e32 v90, 3, v1
	v_lshl_add_u32 v90, v14, 2, v90
	v_lshl_add_u32 v90, v13, 4, v90
	s_lshl_b32 s19, s16, 8
	s_and_b32 s20, s2, 1
	s_mul_i32 s20, s20, 0x3000
	s_add_u32 s19, s19, s20
	v_lshl_add_u32 v90, v90, 2, s19
	s_waitcnt lgkmcnt(0)
	global_load_dword v24, v5, s[4:5]
	global_load_dword v25, v6, s[4:5]
	global_load_dword v26, v7, s[4:5]
	global_load_dword v27, v7, s[4:5] offset:2048
	global_load_dword v28, v8, s[4:5]
	global_load_dword v29, v8, s[4:5] offset:2048
	global_load_dword v30, v9, s[4:5]
	global_load_dword v31, v9, s[4:5] offset:2048
	global_load_dword v32, v10, s[4:5]
	global_load_dword v33, v10, s[4:5] offset:2048
	global_load_dword v34, v11, s[4:5]
	global_load_dwordx4 v[36:39], v16, s[6:7]
	global_load_dwordx4 v[40:43], v17, s[6:7]
	global_load_dwordx4 v[44:47], v18, s[6:7]
	global_load_dwordx4 v[48:51], v19, s[6:7]
	global_load_dword v52, v16, s[6:7] offset:16
	global_load_dword v53, v17, s[6:7] offset:16
	global_load_dword v54, v18, s[6:7] offset:16
	global_load_dword v55, v19, s[6:7] offset:16
	global_load_dword v56, v20, s[8:9]
	v_lshlrev_b32_e32 v21, 2, v0
	v_and_b32_e32 v22, 63, v0
	v_lshlrev_b32_e32 v22, 2, v22
	v_lshlrev_b32_e32 v23, 2, v14
	v_add_u32_e32 v23, 0xc00, v23
	v_lshlrev_b32_e32 v57, 3, v12
	v_lshl_add_u32 v57, v2, 2, v57
	v_add_u32_e32 v57, 0xc00, v57
	v_mul_u32_u24_e32 v58, 0x900000, v12
	v_sub_u32_e32 v58, 0x3b000000, v58
	v_mov_b32_e32 v89, 1.0
	s_mov_b32 s20, 0x01010101
	s_mov_b32 s21, 0x01010101
	s_mov_b32 s30, 0xaaaaaaaa
	s_mov_b32 s31, 0xaaaaaaaa
	s_mov_b32 s32, 0xcccccccc
	s_mov_b32 s33, 0xcccccccc
	s_mov_b32 s34, 0xf0f0f0f0
	s_mov_b32 s35, 0xf0f0f0f0
	s_mov_b32 s36, 0x000f000f
	s_mov_b32 s37, 0x000f000f
	s_mov_b32 s38, 0x00f000f0
	s_mov_b32 s39, 0x00f000f0
	s_mov_b32 s22, 0xffff
	s_mov_b32 s23, 0
	s_waitcnt vmcnt(9)
	v_add_f32_dpp v34, v34, v34 quad_perm:[1,0,3,2] row_mask:0xf bank_mask:0xf
	v_add_f32_e32 v26, v26, v27
	v_add_f32_e32 v28, v28, v29
	v_add_f32_dpp v34, v34, v34 quad_perm:[2,3,0,1] row_mask:0xf bank_mask:0xf
	v_add_f32_e32 v30, v30, v31
	v_add_f32_e32 v32, v32, v33
	v_add_f32_dpp v34, v34, v34 row_half_mirror row_mask:0xf bank_mask:0xf
	v_add_f32_e32 v26, v26, v28
	v_add_f32_e32 v30, v30, v32
	v_mul_f32_e32 v25, 0x3b000000, v25
	v_add_f32_e32 v26, v26, v30
	v_mul_f32_e32 v34, v58, v34
	v_mul_f32_e32 v26, 0x3b000000, v26
	ds_write_b32 v21, v24
	ds_write_b32 v21, v25 offset:1024
	ds_write_b32 v21, v26 offset:2048
	s_mov_b64 exec, s[20:21]
	ds_write_b32 v57, v34
	s_mov_b64 exec, -1
	s_waitcnt lgkmcnt(0)
	s_barrier
	ds_read2st64_b32 v[60:61], v22 offset0:0 offset1:1
	ds_read2st64_b32 v[62:63], v22 offset0:2 offset1:3
	ds_read2st64_b32 v[64:65], v22 offset0:4 offset1:5
	ds_read2st64_b32 v[66:67], v22 offset0:6 offset1:7
	ds_read2st64_b32 v[68:69], v22 offset0:8 offset1:9
	ds_read2st64_b32 v[70:71], v22 offset0:10 offset1:11
	ds_read2_b32 v[72:73], v23 offset0:0 offset1:16
	ds_read2_b32 v[74:75], v23 offset0:4 offset1:20
	ds_read2_b32 v[76:77], v23 offset0:8 offset1:24
	ds_read2_b32 v[78:79], v23 offset0:12 offset1:28
	s_waitcnt vmcnt(0)
	s_waitcnt lgkmcnt(9)
	v_mfma_f32_16x16x4_f32 v[80:83], v36, v60, 0
	v_mfma_f32_16x16x4_f32 v[84:87], v40, v61, 0
	s_waitcnt lgkmcnt(8)
	v_mfma_f32_16x16x4_f32 v[80:83], v44, v62, v[80:83]
	v_mfma_f32_16x16x4_f32 v[84:87], v48, v63, v[84:87]
	s_waitcnt lgkmcnt(7)
	v_mfma_f32_16x16x4_f32 v[80:83], v38, v64, v[80:83]
	v_mfma_f32_16x16x4_f32 v[84:87], v42, v65, v[84:87]
	v_cndmask_b32_e64 v88, 0, v56, s[22:23]
	s_waitcnt lgkmcnt(6)
	v_mfma_f32_16x16x4_f32 v[80:83], v46, v66, v[80:83]
	v_mfma_f32_16x16x4_f32 v[84:87], v50, v67, v[84:87]
	s_waitcnt lgkmcnt(0)
	v_fmac_f32_e32 v88, v37, v72
	v_fmac_f32_e32 v88, v52, v73
	v_fmac_f32_e32 v88, v41, v74
	v_fmac_f32_e32 v88, v53, v75
	v_fmac_f32_e32 v88, v45, v76
	v_fmac_f32_e32 v88, v54, v77
	v_fmac_f32_e32 v88, v49, v78
	v_fmac_f32_e32 v88, v55, v79
	s_waitcnt lgkmcnt(5)
	v_mfma_f32_16x16x4_f32 v[80:83], v39, v68, v[80:83]
	v_mfma_f32_16x16x4_f32 v[84:87], v43, v69, v[84:87]
	s_waitcnt lgkmcnt(4)
	v_mfma_f32_16x16x4_f32 v[80:83], v47, v70, v[80:83]
	v_mfma_f32_16x16x4_f32 v[84:87], v51, v71, v[84:87]
	v_mfma_f32_16x16x4_f32 v[80:83], v88, v89, v[80:83]
	s_nop 7
	s_nop 1
	v_add_f32_e32 v80, v80, v84
	v_add_f32_e32 v81, v81, v85
	v_add_f32_e32 v82, v82, v86
	v_add_f32_e32 v83, v83, v87
	v_max_f32_e32 v80, 0, v80
	v_max_f32_e32 v81, 0, v81
	v_max_f32_e32 v82, 0, v82
	v_max_f32_e32 v83, 0, v83
	global_store_dwordx4 v59, v[80:83], s[10:11] sc1
	v_mul_f32_e32 v84, v80, v80
	v_mul_f32_e32 v85, v81, v81
	v_mul_f32_e32 v86, v82, v82
	v_mul_f32_e32 v87, v83, v83
	v_add_f32_dpp v80, v80, v80 quad_perm:[1,0,3,2] row_mask:0xf bank_mask:0xf
	v_add_f32_dpp v81, v81, v81 quad_perm:[1,0,3,2] row_mask:0xf bank_mask:0xf
	v_add_f32_dpp v82, v82, v82 quad_perm:[1,0,3,2] row_mask:0xf bank_mask:0xf
	v_add_f32_dpp v83, v83, v83 quad_perm:[1,0,3,2] row_mask:0xf bank_mask:0xf
	v_add_f32_dpp v84, v84, v84 quad_perm:[1,0,3,2] row_mask:0xf bank_mask:0xf
	v_add_f32_dpp v85, v85, v85 quad_perm:[1,0,3,2] row_mask:0xf bank_mask:0xf
	v_add_f32_dpp v86, v86, v86 quad_perm:[1,0,3,2] row_mask:0xf bank_mask:0xf
	v_add_f32_dpp v87, v87, v87 quad_perm:[1,0,3,2] row_mask:0xf bank_mask:0xf
	v_add_f32_dpp v80, v80, v80 quad_perm:[2,3,0,1] row_mask:0xf bank_mask:0xf
	v_add_f32_dpp v81, v81, v81 quad_perm:[2,3,0,1] row_mask:0xf bank_mask:0xf
	v_add_f32_dpp v82, v82, v82 quad_perm:[2,3,0,1] row_mask:0xf bank_mask:0xf
	v_add_f32_dpp v83, v83, v83 quad_perm:[2,3,0,1] row_mask:0xf bank_mask:0xf
	v_add_f32_dpp v84, v84, v84 quad_perm:[2,3,0,1] row_mask:0xf bank_mask:0xf
	v_add_f32_dpp v85, v85, v85 quad_perm:[2,3,0,1] row_mask:0xf bank_mask:0xf
	v_add_f32_dpp v86, v86, v86 quad_perm:[2,3,0,1] row_mask:0xf bank_mask:0xf
	v_add_f32_dpp v87, v87, v87 quad_perm:[2,3,0,1] row_mask:0xf bank_mask:0xf
	v_add_f32_dpp v80, v80, v80 row_half_mirror row_mask:0xf bank_mask:0xf
	v_add_f32_dpp v81, v81, v81 row_half_mirror row_mask:0xf bank_mask:0xf
	v_add_f32_dpp v82, v82, v82 row_half_mirror row_mask:0xf bank_mask:0xf
	v_add_f32_dpp v83, v83, v83 row_half_mirror row_mask:0xf bank_mask:0xf
	v_add_f32_dpp v84, v84, v84 row_half_mirror row_mask:0xf bank_mask:0xf
	v_add_f32_dpp v85, v85, v85 row_half_mirror row_mask:0xf bank_mask:0xf
	v_add_f32_dpp v86, v86, v86 row_half_mirror row_mask:0xf bank_mask:0xf
	v_add_f32_dpp v87, v87, v87 row_half_mirror row_mask:0xf bank_mask:0xf
	v_add_f32_dpp v80, v80, v80 row_mirror row_mask:0xf bank_mask:0xf
	v_add_f32_dpp v81, v81, v81 row_mirror row_mask:0xf bank_mask:0xf
	v_add_f32_dpp v82, v82, v82 row_mirror row_mask:0xf bank_mask:0xf
	v_add_f32_dpp v83, v83, v83 row_mirror row_mask:0xf bank_mask:0xf
	v_add_f32_dpp v84, v84, v84 row_mirror row_mask:0xf bank_mask:0xf
	v_add_f32_dpp v85, v85, v85 row_mirror row_mask:0xf bank_mask:0xf
	v_add_f32_dpp v86, v86, v86 row_mirror row_mask:0xf bank_mask:0xf
	v_add_f32_dpp v87, v87, v87 row_mirror row_mask:0xf bank_mask:0xf
	v_cndmask_b32_e64 v80, v80, v81, s[30:31]
	v_cndmask_b32_e64 v82, v82, v83, s[30:31]
	v_cndmask_b32_e64 v84, v84, v85, s[30:31]
	v_cndmask_b32_e64 v86, v86, v87, s[30:31]
	v_cndmask_b32_e64 v80, v80, v82, s[32:33]
	v_cndmask_b32_e64 v84, v84, v86, s[32:33]
	v_cndmask_b32_e64 v80, v80, v84, s[34:35]
	s_mov_b64 exec, s[36:37]
	global_atomic_add_f32 v90, v80, s[12:13]
	s_mov_b64 exec, s[38:39]
	global_atomic_add_f32 v90, v80, s[14:15]
	s_endpgm
